# P0 fold_pool: software prefetch of the next trip's 16 rows into cache with throwaway loads (real loads keep order, vmcnt counts +16)
# speedup vs baseline: 1.0045x; 1.0045x over previous
; #define LAS __attribute__((address_space(3)))
; template <int MODE>
; __device__ __forceinline__ void phase_prologue(const Ctx& P, LAS unsigned char* lds, int vcu, int G) {
;     ...
;     for (int it = gw; it < 32 * 4 * 32; it += NGW) {
;         const int nb = it & 31, g = (it >> 5) & 3, cblk = it >> 7; const int n = nb * 64 + lane, c0 = cblk * 8;
;         const float* wo = P.in[15] + (size_t)(g * 256) * DM + n; const float* pw = P.in[9] + ((size_t)g * 256 + c0) * 256; const float* scl = P.in[10] + g * 256;
;         { const f32x4 s4 = *(const f32x4*)(scl + 4 * lane);
; #pragma unroll
;           for (int q = 0; q < 8; ++q) *(LAS f32x4*)(pwl + q * 256 + 4 * lane) = *(const f32x4*)(pw + q * 256 + 4 * lane) * s4; }
;         asm volatile("s_waitcnt lgkmcnt(0)" ::: "memory");
;         float a[8];
; #pragma unroll
;         for (int cc = 0; cc < 8; ++cc) a[cc] = 0.f;
; #pragma unroll 4
;         for (int d4 = 0; d4 < 64; ++d4) { const f32x4 wv = (f32x4){wo[(size_t)(4 * d4) * DM], wo[(size_t)(4 * d4 + 1) * DM], wo[(size_t)(4 * d4 + 2) * DM], wo[(size_t)(4 * d4 + 3) * DM]};
; #pragma unroll
;             for (int cc = 0; cc < 8; ++cc) { const f32x4 p4 = *(const LAS f32x4*)(pwl + cc * 256 + 4 * d4); a[cc] += (p4[0] * wv[0] + p4[1] * wv[1]) + (p4[2] * wv[2] + p4[3] * wv[3]); } }
.LBB0_38:
	v_lshl_add_u64 v[18:19], v[10:11], 0, s[18:19]
	v_add_co_u32_e64 v154, s[2:3], s27, v18
	v_add_co_u32_e32 v152, vcc, 0x2000, v18
	s_nop 0
	v_addc_co_u32_e64 v155, s[2:3], 0, v19, s[2:3]
	v_add_co_u32_e64 v156, s[2:3], s29, v18
	v_addc_co_u32_e32 v153, vcc, 0, v19, vcc
	s_nop 0
	v_addc_co_u32_e64 v157, s[2:3], 0, v19, s[2:3]
	v_add_co_u32_e64 v158, s[2:3], s30, v18
	v_mov_b32_e32 v2, s4
	s_nop 0
	v_addc_co_u32_e64 v159, s[2:3], 0, v19, s[2:3]
	v_add_co_u32_e64 v160, s[2:3], s31, v18
	v_add_co_u32_e32 v178, vcc, 0x4000, v18
	s_nop 0
	v_addc_co_u32_e64 v161, s[2:3], 0, v19, s[2:3]
	v_add_co_u32_e64 v162, s[2:3], s34, v18
	global_load_dword v20, v[18:19], off
	s_nop 0
	v_addc_co_u32_e64 v163, s[2:3], 0, v19, s[2:3]
	v_add_co_u32_e64 v164, s[2:3], s35, v18
	ds_read_b128 v[24:27], v2
	ds_read_b128 v[28:31], v2 offset:16
	ds_read_b128 v[32:35], v2 offset:32
	ds_read_b128 v[36:39], v2 offset:48
	v_addc_co_u32_e64 v165, s[2:3], 0, v19, s[2:3]
	v_add_co_u32_e64 v166, s[2:3], s38, v18
	ds_read_b128 v[40:43], v2 offset:1024
	ds_read_b128 v[44:47], v2 offset:1040
	ds_read_b128 v[48:51], v2 offset:2048
	ds_read_b128 v[52:55], v2 offset:2064
	ds_read_b128 v[56:59], v2 offset:3072
	ds_read_b128 v[60:63], v2 offset:3088
	ds_read_b128 v[64:67], v2 offset:4096
	ds_read_b128 v[68:71], v2 offset:4112
	ds_read_b128 v[72:75], v2 offset:5120
	ds_read_b128 v[76:79], v2 offset:5136
	ds_read_b128 v[80:83], v2 offset:6144
	ds_read_b128 v[84:87], v2 offset:6160
	ds_read_b128 v[88:91], v2 offset:7168
	ds_read_b128 v[92:95], v2 offset:7184
	v_addc_co_u32_e64 v167, s[2:3], 0, v19, s[2:3]
	v_add_co_u32_e64 v168, s[2:3], s40, v18
	ds_read_b128 v[96:99], v2 offset:1056
	ds_read_b128 v[100:103], v2 offset:1072
	ds_read_b128 v[104:107], v2 offset:2080
	ds_read_b128 v[108:111], v2 offset:2096
	ds_read_b128 v[112:115], v2 offset:3104
	ds_read_b128 v[116:119], v2 offset:3120
	ds_read_b128 v[120:123], v2 offset:4128
	ds_read_b128 v[124:127], v2 offset:4144
	ds_read_b128 v[128:131], v2 offset:5152
	ds_read_b128 v[132:135], v2 offset:5168
	ds_read_b128 v[136:139], v2 offset:6176
	ds_read_b128 v[140:143], v2 offset:6192
	ds_read_b128 v[144:147], v2 offset:7200
	ds_read_b128 v[148:151], v2 offset:7216
	v_addc_co_u32_e64 v169, s[2:3], 0, v19, s[2:3]
	v_add_co_u32_e64 v170, s[2:3], s41, v18
	v_addc_co_u32_e32 v179, vcc, 0, v19, vcc
	s_nop 0
	v_addc_co_u32_e64 v171, s[2:3], 0, v19, s[2:3]
	v_add_co_u32_e64 v172, s[2:3], s42, v18
	s_add_u32 s18, s18, 0x20000
	s_nop 0
	v_addc_co_u32_e64 v173, s[2:3], 0, v19, s[2:3]
	v_add_co_u32_e64 v174, s[2:3], s43, v18
	s_addc_u32 s19, s19, 0
	s_nop 0
	v_addc_co_u32_e64 v175, s[2:3], 0, v19, s[2:3]
	v_add_co_u32_e64 v176, s[2:3], s44, v18
	v_add_co_u32_e32 v18, vcc, 0x6000, v18
	s_nop 0
	v_addc_co_u32_e64 v177, s[2:3], 0, v19, s[2:3]
	global_load_dword v154, v[154:155], off
	s_nop 0
	global_load_dword v156, v[156:157], off
	s_nop 0
	global_load_dword v158, v[158:159], off
	s_nop 0
	global_load_dword v2, v[160:161], off
	s_nop 0
	global_load_dword v160, v[162:163], off
	s_nop 0
	global_load_dword v162, v[164:165], off
	s_nop 0
	global_load_dword v164, v[166:167], off
	s_nop 0
	global_load_dword v166, v[168:169], off
	s_nop 0
	global_load_dword v168, v[170:171], off
	s_nop 0
	global_load_dword v170, v[172:173], off
	s_nop 0
	global_load_dword v172, v[174:175], off
	s_nop 0
	global_load_dword v174, v[176:177], off
	v_addc_co_u32_e32 v19, vcc, 0, v19, vcc
	global_load_dword v152, v[152:153], off
	s_nop 0
	global_load_dword v176, v[178:179], off
	s_nop 0
	global_load_dword v18, v[18:19], off
	s_cmp_eq_u32 s18, 0x200000
	s_cselect_b32 s2, 0x1e0000, s18
	s_mov_b32 s3, s19
	s_mov_b64 s[100:101], 0x2000
	v_lshl_add_u64 v[252:253], v[10:11], 0, s[2:3]
	global_load_dword v255, v[252:253], off
	v_lshl_add_u64 v[252:253], v[252:253], 0, s[100:101]
	global_load_dword v255, v[252:253], off
	v_lshl_add_u64 v[252:253], v[252:253], 0, s[100:101]
	global_load_dword v255, v[252:253], off
	v_lshl_add_u64 v[252:253], v[252:253], 0, s[100:101]
	global_load_dword v255, v[252:253], off
	v_lshl_add_u64 v[252:253], v[252:253], 0, s[100:101]
	global_load_dword v255, v[252:253], off
	v_lshl_add_u64 v[252:253], v[252:253], 0, s[100:101]
	global_load_dword v255, v[252:253], off
	v_lshl_add_u64 v[252:253], v[252:253], 0, s[100:101]
	global_load_dword v255, v[252:253], off
	v_lshl_add_u64 v[252:253], v[252:253], 0, s[100:101]
	global_load_dword v255, v[252:253], off
	v_lshl_add_u64 v[252:253], v[252:253], 0, s[100:101]
	global_load_dword v255, v[252:253], off
	v_lshl_add_u64 v[252:253], v[252:253], 0, s[100:101]
	global_load_dword v255, v[252:253], off
	v_lshl_add_u64 v[252:253], v[252:253], 0, s[100:101]
	global_load_dword v255, v[252:253], off
	v_lshl_add_u64 v[252:253], v[252:253], 0, s[100:101]
	global_load_dword v255, v[252:253], off
	v_lshl_add_u64 v[252:253], v[252:253], 0, s[100:101]
	global_load_dword v255, v[252:253], off
	v_lshl_add_u64 v[252:253], v[252:253], 0, s[100:101]
	global_load_dword v255, v[252:253], off
	v_lshl_add_u64 v[252:253], v[252:253], 0, s[100:101]
	global_load_dword v255, v[252:253], off
	v_lshl_add_u64 v[252:253], v[252:253], 0, s[100:101]
	global_load_dword v255, v[252:253], off
	s_waitcnt lgkmcnt(14)
; #define LAS __attribute__((address_space(3)))
; template <int MODE>
; __device__ __forceinline__ void phase_prologue(const Ctx& P, LAS unsigned char* lds, int vcu, int G) {
;     ...
;         for (int d4 = 0; d4 < 64; ++d4) { const f32x4 wv = (f32x4){wo[(size_t)(4 * d4) * DM], wo[(size_t)(4 * d4 + 1) * DM], wo[(size_t)(4 * d4 + 2) * DM], wo[(size_t)(4 * d4 + 3) * DM]};
; #pragma unroll
;             for (int cc = 0; cc < 8; ++cc) { const f32x4 p4 = *(const LAS f32x4*)(pwl + cc * 256 + 4 * d4); a[cc] += (p4[0] * wv[0] + p4[1] * wv[1]) + (p4[2] * wv[2] + p4[3] * wv[3]); } }
	v_mov_b32_e32 v178, v24
	v_mov_b32_e32 v179, v40
	v_mov_b32_e32 v40, v25
	v_mov_b32_e32 v24, v26
	v_mov_b32_e32 v25, v42
	v_mov_b32_e32 v42, v27
	v_mov_b32_e32 v26, v48
	v_mov_b32_e32 v27, v56
	v_mov_b32_e32 v56, v49
	v_mov_b32_e32 v48, v50
	v_mov_b32_e32 v49, v58
	v_mov_b32_e32 v58, v51
	v_mov_b32_e32 v50, v64
	v_mov_b32_e32 v51, v72
	v_mov_b32_e32 v72, v65
	v_mov_b32_e32 v64, v66
	v_mov_b32_e32 v65, v74
	v_mov_b32_e32 v74, v67
	v_mov_b32_e32 v66, v89
	v_mov_b32_e32 v67, v90
	v_mov_b32_e32 v89, v91
	v_mov_b32_e32 v90, v28
	v_mov_b32_e32 v91, v44
	v_mov_b32_e32 v44, v29
	v_mov_b32_e32 v28, v30
	v_mov_b32_e32 v29, v46
	v_mov_b32_e32 v46, v31
	v_mov_b32_e32 v30, v52
	v_mov_b32_e32 v31, v60
	v_mov_b32_e32 v60, v53
	v_mov_b32_e32 v52, v54
	v_mov_b32_e32 v53, v62
	v_mov_b32_e32 v62, v55
	v_mov_b32_e32 v54, v68
	v_mov_b32_e32 v55, v76
	v_mov_b32_e32 v76, v69
	v_mov_b32_e32 v68, v70
	v_mov_b32_e32 v69, v78
	v_mov_b32_e32 v78, v71
	v_mov_b32_e32 v70, v93
	v_mov_b32_e32 v93, v95
	s_waitcnt lgkmcnt(13)
	v_mov_b32_e32 v95, v96
	v_mov_b32_e32 v96, v33
	v_mov_b32_e32 v33, v98
	v_mov_b32_e32 v98, v35
	s_waitcnt lgkmcnt(9)
	v_mov_b32_e32 v35, v112
	v_mov_b32_e32 v112, v105
	v_mov_b32_e32 v105, v114
	v_mov_b32_e32 v114, v107
	s_waitcnt lgkmcnt(5)
	v_mov_b32_e32 v107, v128
	v_mov_b32_e32 v128, v121
	v_mov_b32_e32 v121, v130
	v_mov_b32_e32 v130, v123
	v_mov_b32_e32 v71, v94
	v_mov_b32_e32 v94, v32
	v_mov_b32_e32 v32, v34
	v_mov_b32_e32 v34, v104
	v_mov_b32_e32 v104, v106
	v_mov_b32_e32 v106, v120
	v_mov_b32_e32 v120, v122
	s_waitcnt lgkmcnt(1)
	v_mov_b32_e32 v122, v145
	v_mov_b32_e32 v145, v147
	v_mov_b32_e32 v147, v100
	v_mov_b32_e32 v100, v37
	v_mov_b32_e32 v37, v102
	s_waitcnt vmcnt(29)
	v_pk_mul_f32 v[44:45], v[156:157], v[44:45] op_sel_hi:[0,1]
	v_pk_mul_f32 v[76:77], v[156:157], v[76:77] op_sel_hi:[0,1]
	s_waitcnt vmcnt(27)
	v_pk_mul_f32 v[46:47], v[2:3], v[46:47] op_sel_hi:[0,1]
	v_pk_mul_f32 v[62:63], v[2:3], v[62:63] op_sel_hi:[0,1]
	v_pk_mul_f32 v[78:79], v[2:3], v[78:79] op_sel_hi:[0,1]
	s_waitcnt vmcnt(25)
	v_pk_mul_f32 v[128:129], v[162:163], v[128:129] op_sel_hi:[0,1]
	s_waitcnt vmcnt(23)
	v_pk_mul_f32 v[130:131], v[166:167], v[130:131] op_sel_hi:[0,1]
	v_mov_b32_e32 v102, v39
	v_pk_mul_f32 v[60:61], v[156:157], v[60:61] op_sel_hi:[0,1]
	v_pk_fma_f32 v[44:45], v[154:155], v[90:91], v[44:45] op_sel_hi:[0,1,1]
	v_pk_fma_f32 v[28:29], v[158:159], v[28:29], v[46:47] op_sel_hi:[0,1,1]
	v_pk_fma_f32 v[46:47], v[158:159], v[52:53], v[62:63] op_sel_hi:[0,1,1]
	v_pk_fma_f32 v[52:53], v[154:155], v[54:55], v[76:77] op_sel_hi:[0,1,1]
	s_waitcnt vmcnt(18)
	v_pk_mul_f32 v[40:41], v[152:153], v[40:41] op_sel_hi:[0,1]
	v_pk_mul_f32 v[56:57], v[152:153], v[56:57] op_sel_hi:[0,1]
	v_pk_mul_f32 v[72:73], v[152:153], v[72:73] op_sel_hi:[0,1]
	v_mul_f32_e32 v190, v152, v81
	v_pk_fma_f32 v[54:55], v[158:159], v[68:69], v[78:79] op_sel_hi:[0,1,1]
	v_pk_fma_f32 v[68:69], v[160:161], v[106:107], v[128:129] op_sel_hi:[0,1,1]
	v_pk_fma_f32 v[76:77], v[164:165], v[120:121], v[130:131] op_sel_hi:[0,1,1]
	v_pk_fma_f32 v[40:41], v[20:21], v[178:179], v[40:41] op_sel_hi:[0,1,1]
	v_pk_fma_f32 v[26:27], v[20:21], v[26:27], v[56:57] op_sel_hi:[0,1,1]
	v_pk_fma_f32 v[50:51], v[20:21], v[50:51], v[72:73] op_sel_hi:[0,1,1]
	v_mov_b32_e32 v21, v152
	v_mov_b32_e32 v123, v146
	v_mov_b32_e32 v146, v36
	v_mov_b32_e32 v36, v38
	v_mov_b32_e32 v39, v116
	v_mov_b32_e32 v116, v109
	v_mov_b32_e32 v109, v118
	v_mov_b32_e32 v118, v111
	v_mov_b32_e32 v111, v132
	v_mov_b32_e32 v132, v125
	v_mov_b32_e32 v125, v134
	v_mov_b32_e32 v134, v127
	s_waitcnt lgkmcnt(0)
	v_mov_b32_e32 v127, v150
	v_mul_f32_e32 v150, v156, v85
	v_pk_mul_f32 v[96:97], v[162:163], v[96:97] op_sel_hi:[0,1]
	v_pk_mul_f32 v[112:113], v[162:163], v[112:113] op_sel_hi:[0,1]
	v_pk_mul_f32 v[100:101], v[170:171], v[100:101] op_sel_hi:[0,1]
	v_pk_mul_f32 v[102:103], v[174:175], v[102:103] op_sel_hi:[0,1]
	v_pk_fma_f32 v[30:31], v[154:155], v[30:31], v[60:61] op_sel_hi:[0,1,1]
	v_mov_b32_e32 v155, v156
	v_pk_add_f32 v[28:29], v[44:45], v[28:29]
	v_pk_add_f32 v[44:45], v[52:53], v[54:55]
	v_pk_add_f32 v[54:55], v[68:69], v[76:77]
	s_waitcnt vmcnt(16)
; #define LAS __attribute__((address_space(3)))
; __device__ __forceinline__ unsigned cvt_pk_bf16(float lo, float hi) { unsigned r; asm("v_cvt_pk_bf16_f32 %0, %1, %2" : "=v"(r) : "v"(lo), "v"(hi)); return r; }
; template <int MODE>
; __device__ __forceinline__ void phase_prologue(const Ctx& P, LAS unsigned char* lds, int vcu, int G) {
;     ...
;         for (int d4 = 0; d4 < 64; ++d4) { const f32x4 wv = (f32x4){wo[(size_t)(4 * d4) * DM], wo[(size_t)(4 * d4 + 1) * DM], wo[(size_t)(4 * d4 + 2) * DM], wo[(size_t)(4 * d4 + 3) * DM]};
; #pragma unroll
;             for (int cc = 0; cc < 8; ++cc) { const f32x4 p4 = *(const LAS f32x4*)(pwl + cc * 256 + 4 * d4); a[cc] += (p4[0] * wv[0] + p4[1] * wv[1]) + (p4[2] * wv[2] + p4[3] * wv[3]); } }
;         u32x4 w; w.x = cvt_pk_bf16(a[0], a[1]); w.y = cvt_pk_bf16(a[2], a[3]); w.z = cvt_pk_bf16(a[4], a[5]); w.w = cvt_pk_bf16(a[6], a[7]);
;         *(u32x4*)((bf16_t*)(ws + WS_WEOUT) + (size_t)n * DM + g * 256 + c0) = w;
;         asm volatile("s_waitcnt lgkmcnt(0)" ::: "memory");
;     }
	v_pk_mul_f32 v[42:43], v[18:19], v[42:43] op_sel_hi:[0,1]
	v_pk_mul_f32 v[58:59], v[18:19], v[58:59] op_sel_hi:[0,1]
	v_pk_mul_f32 v[74:75], v[18:19], v[74:75] op_sel_hi:[0,1]
	v_pk_fma_f32 v[76:77], v[20:21], v[80:81], v[190:191] op_sel_hi:[1,1,0]
	v_mov_b32_e32 v21, v18
	v_mov_b32_e32 v38, v108
	v_mov_b32_e32 v108, v110
	v_mov_b32_e32 v110, v124
	v_mul_f32_e32 v180, v2, v87
	v_mul_f32_e32 v182, v162, v137
	v_pk_mul_f32 v[116:117], v[170:171], v[116:117] op_sel_hi:[0,1]
	v_pk_mul_f32 v[132:133], v[170:171], v[132:133] op_sel_hi:[0,1]
	v_mov_b32_e32 v159, v2
	v_pk_fma_f32 v[60:61], v[160:161], v[94:95], v[96:97] op_sel_hi:[0,1,1]
	v_pk_fma_f32 v[34:35], v[160:161], v[34:35], v[112:113] op_sel_hi:[0,1,1]
	v_mov_b32_e32 v161, v162
	v_pk_fma_f32 v[78:79], v[168:169], v[146:147], v[100:101] op_sel_hi:[0,1,1]
	v_pk_fma_f32 v[36:37], v[172:173], v[36:37], v[102:103] op_sel_hi:[0,1,1]
	v_mov_b32_e32 v153, v176
	v_pk_add_f32 v[30:31], v[30:31], v[46:47]
	v_pk_fma_f32 v[46:47], v[154:155], v[84:85], v[150:151] op_sel_hi:[1,1,0]
	v_mov_b32_e32 v155, v2
	v_mul_f32_e32 v2, v18, v83
	v_pk_fma_f32 v[24:25], v[176:177], v[24:25], v[42:43] op_sel_hi:[0,1,1]
	v_pk_fma_f32 v[42:43], v[176:177], v[48:49], v[58:59] op_sel_hi:[0,1,1]
	v_pk_fma_f32 v[48:49], v[176:177], v[64:65], v[74:75] op_sel_hi:[0,1,1]
	v_mov_b32_e32 v177, v18
	v_pk_mul_f32 v[18:19], v[20:21], v[88:89]
	v_mov_b32_e32 v157, v158
	v_pk_mul_f32 v[98:99], v[166:167], v[98:99] op_sel_hi:[0,1]
	v_pk_mul_f32 v[114:115], v[166:167], v[114:115] op_sel_hi:[0,1]
	v_mul_f32_e32 v186, v170, v141
	v_pk_fma_f32 v[38:39], v[168:169], v[38:39], v[116:117] op_sel_hi:[0,1,1]
	v_pk_fma_f32 v[94:95], v[168:169], v[110:111], v[132:133] op_sel_hi:[0,1,1]
	v_mov_b32_e32 v169, v170
	v_pk_fma_f32 v[56:57], v[160:161], v[136:137], v[182:183] op_sel_hi:[1,1,0]
	v_mov_b32_e32 v161, v166
	v_pk_add_f32 v[36:37], v[78:79], v[36:37]
	v_pk_mul_f32 v[78:79], v[154:155], v[92:93]
	v_pk_add_f32 v[26:27], v[26:27], v[42:43]
	v_pk_fma_f32 v[42:43], v[176:177], v[82:83], v[2:3] op_sel_hi:[1,1,0]
	v_pk_fma_f32 v[18:19], v[152:153], v[66:67], v[18:19]
	v_mov_b32_e32 v124, v126
	v_mov_b32_e32 v126, v149
	v_mov_b32_e32 v149, v151
	v_mul_f32_e32 v184, v166, v139
	v_mov_b32_e32 v163, v164
	v_pk_mul_f32 v[118:119], v[174:175], v[118:119] op_sel_hi:[0,1]
	v_pk_mul_f32 v[134:135], v[174:175], v[134:135] op_sel_hi:[0,1]
	v_pk_fma_f32 v[32:33], v[164:165], v[32:33], v[98:99] op_sel_hi:[0,1,1]
	v_pk_fma_f32 v[62:63], v[164:165], v[104:105], v[114:115] op_sel_hi:[0,1,1]
	v_mov_b32_e32 v165, v166
	v_pk_fma_f32 v[52:53], v[158:159], v[86:87], v[180:181] op_sel_hi:[1,1,0]
	v_pk_fma_f32 v[68:69], v[168:169], v[140:141], v[186:187] op_sel_hi:[1,1,0]
	v_mov_b32_e32 v169, v174
	v_pk_mul_f32 v[80:81], v[160:161], v[144:145]
	v_pk_fma_f32 v[20:21], v[156:157], v[70:71], v[78:79]
	v_mov_b32_e32 v77, v18
	v_mov_b32_e32 v43, v19
	v_mul_f32_e32 v188, v174, v143
	v_mov_b32_e32 v171, v172
	v_pk_fma_f32 v[90:91], v[172:173], v[108:109], v[118:119] op_sel_hi:[0,1,1]
	v_pk_fma_f32 v[96:97], v[172:173], v[124:125], v[134:135] op_sel_hi:[0,1,1]
	v_mov_b32_e32 v173, v174
	v_pk_add_f32 v[32:33], v[60:61], v[32:33]
	v_pk_fma_f32 v[60:61], v[164:165], v[138:139], v[184:185] op_sel_hi:[1,1,0]
	v_pk_mul_f32 v[84:85], v[168:169], v[148:149]
	v_pk_fma_f32 v[58:59], v[162:163], v[122:123], v[80:81]
	v_pk_add_f32 v[24:25], v[40:41], v[24:25]
	v_pk_add_f32 v[40:41], v[50:51], v[48:49]
	v_mov_b32_e32 v47, v20
	v_mov_b32_e32 v53, v21
	v_pk_add_f32 v[16:17], v[16:17], v[26:27]
	v_pk_add_f32 v[26:27], v[76:77], v[42:43]
	v_pk_fma_f32 v[72:73], v[172:173], v[142:143], v[188:189] op_sel_hi:[1,1,0]
	v_pk_fma_f32 v[64:65], v[170:171], v[126:127], v[84:85]
	v_mov_b32_e32 v57, v58
	v_mov_b32_e32 v61, v59
	v_pk_add_f32 v[12:13], v[12:13], v[24:25]
	v_pk_add_f32 v[14:15], v[14:15], v[40:41]
	v_pk_add_f32 v[18:19], v[46:47], v[52:53]
	v_pk_add_f32 v[8:9], v[8:9], v[26:27]
	v_pk_add_f32 v[34:35], v[34:35], v[62:63]
	v_mov_b32_e32 v69, v64
	v_mov_b32_e32 v73, v65
	v_pk_add_f32 v[20:21], v[56:57], v[60:61]
	v_pk_add_f32 v[12:13], v[12:13], v[28:29]
	v_pk_add_f32 v[16:17], v[16:17], v[30:31]
	v_pk_add_f32 v[14:15], v[14:15], v[44:45]
	v_pk_add_f32 v[8:9], v[8:9], v[18:19]
	s_add_i32 s4, s4, 64
	v_pk_add_f32 v[38:39], v[38:39], v[90:91]
	v_pk_add_f32 v[62:63], v[94:95], v[96:97]
	v_pk_add_f32 v[24:25], v[68:69], v[72:73]
	v_pk_add_f32 v[12:13], v[12:13], v[32:33]
	v_pk_add_f32 v[16:17], v[16:17], v[34:35]
	v_pk_add_f32 v[14:15], v[14:15], v[54:55]
	v_pk_add_f32 v[8:9], v[8:9], v[20:21]
	s_cmp_eq_u32 s18, 0x200000
	v_pk_add_f32 v[12:13], v[12:13], v[36:37]
	v_pk_add_f32 v[16:17], v[16:17], v[38:39]
	v_pk_add_f32 v[14:15], v[14:15], v[62:63]
	v_pk_add_f32 v[8:9], v[8:9], v[24:25]
	s_cbranch_scc0 .LBB0_38
	s_lshl_b32 s2, s45, 6
	s_and_b32 s2, s2, 0x7c0
	v_or_b32_e32 v2, s2, v1
	v_lshlrev_b32_e32 v2, 12, v2
	v_cvt_pk_bf16_f32 v10, v12, v13
	v_cvt_pk_bf16_f32 v13, v8, v9
	v_lshl_add_u64 v[8:9], s[14:15], 0, v[2:3]
	s_lshl_b32 s4, s46, 1
	v_lshl_add_u64 v[8:9], v[8:9], 0, s[4:5]
	v_lshl_add_u64 v[8:9], s[16:17], 1, v[8:9]
	v_cvt_pk_bf16_f32 v11, v16, v17
	v_cvt_pk_bf16_f32 v12, v14, v15
	global_store_dwordx4 v[8:9], v[10:13], off
	s_waitcnt lgkmcnt(0)
	s_add_i32 s45, s45, s20
	s_add_i32 s22, s22, s23
	s_add_i32 s24, s24, s25
	s_cmpk_gt_i32 s45, 0xfff
	s_cbranch_scc0 .LBB0_37

; #define LAS __attribute__((address_space(3)))
; template <int MODE>
; __device__ __forceinline__ void phase_prologue(const Ctx& P, LAS unsigned char* lds, int vcu, int G) {
;     ...
;         for (int d4 = 0; d4 < 64; ++d4) { const f32x4 wv = (f32x4){wo[(size_t)(4 * d4) * DM], wo[(size_t)(4 * d4 + 1) * DM], wo[(size_t)(4 * d4 + 2) * DM], wo[(size_t)(4 * d4 + 3) * DM]};
; #pragma unroll
;             for (int cc = 0; cc < 8; ++cc) { const f32x4 p4 = *(const LAS f32x4*)(pwl + cc * 256 + 4 * d4); a[cc] += (p4[0] * wv[0] + p4[1] * wv[1]) + (p4[2] * wv[2] + p4[3] * wv[3]); } }
.LBB0_294:
	v_lshl_add_u64 v[66:67], v[58:59], 0, s[14:15]
	v_add_co_u32_e64 v154, s[2:3], s23, v66
	v_add_co_u32_e32 v152, vcc, 0x2000, v66
	s_nop 0
	v_addc_co_u32_e64 v155, s[2:3], 0, v67, s[2:3]
	v_add_co_u32_e64 v156, s[2:3], s24, v66
	v_addc_co_u32_e32 v153, vcc, 0, v67, vcc
	s_nop 0
	v_addc_co_u32_e64 v157, s[2:3], 0, v67, s[2:3]
	v_add_co_u32_e64 v158, s[2:3], s25, v66
	v_mov_b32_e32 v50, s4
	s_nop 0
	v_addc_co_u32_e64 v159, s[2:3], 0, v67, s[2:3]
	v_add_co_u32_e64 v160, s[2:3], s26, v66
	v_add_co_u32_e32 v178, vcc, 0x4000, v66
	s_nop 0
	v_addc_co_u32_e64 v161, s[2:3], 0, v67, s[2:3]
	v_add_co_u32_e64 v162, s[2:3], s27, v66
	global_load_dword v68, v[66:67], off
	s_nop 0
	v_addc_co_u32_e64 v163, s[2:3], 0, v67, s[2:3]
	v_add_co_u32_e64 v164, s[2:3], s28, v66
	ds_read_b128 v[72:75], v50
	ds_read_b128 v[76:79], v50 offset:16
	ds_read_b128 v[80:83], v50 offset:32
	ds_read_b128 v[84:87], v50 offset:48
	v_addc_co_u32_e64 v165, s[2:3], 0, v67, s[2:3]
	v_add_co_u32_e64 v166, s[2:3], s29, v66
	ds_read_b128 v[10:13], v50 offset:1024
	ds_read_b128 v[34:37], v50 offset:1040
	ds_read_b128 v[88:91], v50 offset:2048
	ds_read_b128 v[92:95], v50 offset:2064
	ds_read_b128 v[14:17], v50 offset:3072
	ds_read_b128 v[38:41], v50 offset:3088
	ds_read_b128 v[96:99], v50 offset:4096
	ds_read_b128 v[100:103], v50 offset:4112
	ds_read_b128 v[18:21], v50 offset:5120
	ds_read_b128 v[42:45], v50 offset:5136
	ds_read_b128 v[2:5], v50 offset:6144
	ds_read_b128 v[26:29], v50 offset:6160
	ds_read_b128 v[6:9], v50 offset:7168
	ds_read_b128 v[22:25], v50 offset:7184
	v_addc_co_u32_e64 v167, s[2:3], 0, v67, s[2:3]
	v_add_co_u32_e64 v168, s[2:3], s30, v66
	ds_read_b128 v[104:107], v50 offset:1056
	ds_read_b128 v[46:49], v50 offset:1072
	ds_read_b128 v[108:111], v50 offset:2080
	ds_read_b128 v[112:115], v50 offset:2096
	ds_read_b128 v[116:119], v50 offset:3104
	ds_read_b128 v[120:123], v50 offset:3120
	ds_read_b128 v[124:127], v50 offset:4128
	ds_read_b128 v[128:131], v50 offset:4144
	ds_read_b128 v[132:135], v50 offset:5152
	ds_read_b128 v[136:139], v50 offset:5168
	ds_read_b128 v[30:33], v50 offset:6176
	ds_read_b128 v[140:143], v50 offset:6192
	ds_read_b128 v[144:147], v50 offset:7200
	ds_read_b128 v[148:151], v50 offset:7216
	v_addc_co_u32_e64 v169, s[2:3], 0, v67, s[2:3]
	v_add_co_u32_e64 v170, s[2:3], s31, v66
	v_addc_co_u32_e32 v179, vcc, 0, v67, vcc
	s_nop 0
	v_addc_co_u32_e64 v171, s[2:3], 0, v67, s[2:3]
	v_add_co_u32_e64 v172, s[2:3], s34, v66
	s_add_u32 s14, s14, 0x20000
	s_nop 0
	v_addc_co_u32_e64 v173, s[2:3], 0, v67, s[2:3]
	v_add_co_u32_e64 v174, s[2:3], s35, v66
	s_addc_u32 s15, s15, 0
	s_nop 0
	v_addc_co_u32_e64 v175, s[2:3], 0, v67, s[2:3]
	v_add_co_u32_e64 v176, s[2:3], s38, v66
	v_add_co_u32_e32 v66, vcc, 0x6000, v66
	s_nop 0
	v_addc_co_u32_e64 v177, s[2:3], 0, v67, s[2:3]
	global_load_dword v156, v[156:157], off
	s_nop 0
	global_load_dword v158, v[158:159], off
	s_nop 0
	global_load_dword v50, v[160:161], off
	s_nop 0
	global_load_dword v160, v[162:163], off
	s_nop 0
	global_load_dword v162, v[164:165], off
	s_nop 0
	global_load_dword v164, v[166:167], off
	s_nop 0
	global_load_dword v166, v[168:169], off
	s_nop 0
	global_load_dword v154, v[154:155], off
	s_nop 0
	global_load_dword v168, v[172:173], off
	s_nop 0
	global_load_dword v172, v[174:175], off
	s_nop 0
	global_load_dword v174, v[176:177], off
	s_nop 0
	global_load_dword v170, v[170:171], off
	v_addc_co_u32_e32 v67, vcc, 0, v67, vcc
	global_load_dword v152, v[152:153], off
	s_nop 0
	global_load_dword v176, v[178:179], off
	s_nop 0
	global_load_dword v66, v[66:67], off
	s_cmp_eq_u32 s14, 0x200000
	s_cselect_b32 s2, 0x1e0000, s14
	s_mov_b32 s3, s15
	s_mov_b64 s[100:101], 0x2000
	v_lshl_add_u64 v[252:253], v[58:59], 0, s[2:3]
	global_load_dword v255, v[252:253], off
	v_lshl_add_u64 v[252:253], v[252:253], 0, s[100:101]
	global_load_dword v255, v[252:253], off
	v_lshl_add_u64 v[252:253], v[252:253], 0, s[100:101]
	global_load_dword v255, v[252:253], off
	v_lshl_add_u64 v[252:253], v[252:253], 0, s[100:101]
	global_load_dword v255, v[252:253], off
	v_lshl_add_u64 v[252:253], v[252:253], 0, s[100:101]
	global_load_dword v255, v[252:253], off
	v_lshl_add_u64 v[252:253], v[252:253], 0, s[100:101]
	global_load_dword v255, v[252:253], off
	v_lshl_add_u64 v[252:253], v[252:253], 0, s[100:101]
	global_load_dword v255, v[252:253], off
	v_lshl_add_u64 v[252:253], v[252:253], 0, s[100:101]
	global_load_dword v255, v[252:253], off
	v_lshl_add_u64 v[252:253], v[252:253], 0, s[100:101]
	global_load_dword v255, v[252:253], off
	v_lshl_add_u64 v[252:253], v[252:253], 0, s[100:101]
	global_load_dword v255, v[252:253], off
	v_lshl_add_u64 v[252:253], v[252:253], 0, s[100:101]
	global_load_dword v255, v[252:253], off
	v_lshl_add_u64 v[252:253], v[252:253], 0, s[100:101]
	global_load_dword v255, v[252:253], off
	v_lshl_add_u64 v[252:253], v[252:253], 0, s[100:101]
	global_load_dword v255, v[252:253], off
	v_lshl_add_u64 v[252:253], v[252:253], 0, s[100:101]
	global_load_dword v255, v[252:253], off
	v_lshl_add_u64 v[252:253], v[252:253], 0, s[100:101]
	global_load_dword v255, v[252:253], off
	v_lshl_add_u64 v[252:253], v[252:253], 0, s[100:101]
	global_load_dword v255, v[252:253], off
	s_waitcnt lgkmcnt(14)
; #define LAS __attribute__((address_space(3)))
; template <int MODE>
; __device__ __forceinline__ void phase_prologue(const Ctx& P, LAS unsigned char* lds, int vcu, int G) {
;     ...
;         for (int d4 = 0; d4 < 64; ++d4) { const f32x4 wv = (f32x4){wo[(size_t)(4 * d4) * DM], wo[(size_t)(4 * d4 + 1) * DM], wo[(size_t)(4 * d4 + 2) * DM], wo[(size_t)(4 * d4 + 3) * DM]};
; #pragma unroll
;             for (int cc = 0; cc < 8; ++cc) { const f32x4 p4 = *(const LAS f32x4*)(pwl + cc * 256 + 4 * d4); a[cc] += (p4[0] * wv[0] + p4[1] * wv[1]) + (p4[2] * wv[2] + p4[3] * wv[3]); } }
	v_mov_b32_e32 v179, v10
	v_mov_b32_e32 v10, v73
	v_mov_b32_e32 v73, v12
	v_mov_b32_e32 v12, v75
	v_mov_b32_e32 v75, v14
	v_mov_b32_e32 v14, v89
	v_mov_b32_e32 v89, v16
	v_mov_b32_e32 v16, v91
	v_mov_b32_e32 v91, v18
	v_mov_b32_e32 v18, v97
	v_mov_b32_e32 v97, v20
	v_mov_b32_e32 v20, v99
	v_mov_b32_e32 v99, v34
	v_mov_b32_e32 v34, v77
	v_mov_b32_e32 v77, v36
	v_mov_b32_e32 v36, v79
	v_mov_b32_e32 v79, v38
	v_mov_b32_e32 v38, v93
	v_mov_b32_e32 v93, v40
	v_mov_b32_e32 v40, v95
	v_mov_b32_e32 v95, v42
	v_mov_b32_e32 v42, v101
	v_mov_b32_e32 v101, v44
	v_mov_b32_e32 v44, v103
	v_mov_b32_e32 v178, v72
	v_mov_b32_e32 v72, v74
	v_mov_b32_e32 v74, v88
	v_mov_b32_e32 v88, v90
	v_mov_b32_e32 v90, v96
	v_mov_b32_e32 v96, v98
	v_mov_b32_e32 v98, v76
	v_mov_b32_e32 v76, v78
	v_mov_b32_e32 v78, v92
	v_mov_b32_e32 v92, v94
	v_mov_b32_e32 v94, v100
	v_mov_b32_e32 v100, v102
	s_waitcnt lgkmcnt(13)
	v_mov_b32_e32 v103, v104
	v_mov_b32_e32 v104, v81
	v_mov_b32_e32 v81, v106
	v_mov_b32_e32 v106, v83
	s_waitcnt lgkmcnt(9)
	v_mov_b32_e32 v83, v116
	v_mov_b32_e32 v116, v109
	v_mov_b32_e32 v109, v118
	v_mov_b32_e32 v118, v111
	s_waitcnt lgkmcnt(5)
	v_mov_b32_e32 v111, v132
	v_mov_b32_e32 v132, v125
	v_mov_b32_e32 v102, v80
	v_mov_b32_e32 v80, v82
	v_mov_b32_e32 v82, v108
	v_mov_b32_e32 v108, v110
	v_mov_b32_e32 v110, v124
	v_mov_b32_e32 v124, v126
	v_mov_b32_e32 v125, v134
	v_mov_b32_e32 v134, v127
	v_mov_b32_e32 v126, v84
	v_mov_b32_e32 v127, v46
	v_mov_b32_e32 v46, v85
	v_mov_b32_e32 v84, v86
	v_mov_b32_e32 v85, v48
	v_mov_b32_e32 v48, v87
	v_mov_b32_e32 v86, v112
	v_mov_b32_e32 v87, v120
	v_mov_b32_e32 v120, v113
	v_mov_b32_e32 v112, v114
	s_waitcnt vmcnt(30)
	v_pk_mul_f32 v[34:35], v[156:157], v[34:35] op_sel_hi:[0,1]
	v_pk_mul_f32 v[38:39], v[156:157], v[38:39] op_sel_hi:[0,1]
	s_waitcnt vmcnt(28)
	v_pk_mul_f32 v[44:45], v[50:51], v[44:45] op_sel_hi:[0,1]
	v_pk_mul_f32 v[42:43], v[156:157], v[42:43] op_sel_hi:[0,1]
	v_pk_fma_f32 v[44:45], v[158:159], v[100:101], v[44:45] op_sel_hi:[0,1,1]
	v_mov_b32_e32 v113, v122
	v_mov_b32_e32 v122, v115
	v_mov_b32_e32 v114, v128
	s_waitcnt lgkmcnt(4)
	v_mov_b32_e32 v115, v136
	v_mov_b32_e32 v136, v129
	v_mov_b32_e32 v128, v130
	v_mov_b32_e32 v130, v7
	v_mov_b32_e32 v7, v9
	v_mov_b32_e32 v9, v24
	s_waitcnt vmcnt(18)
	v_pk_mul_f32 v[10:11], v[152:153], v[10:11] op_sel_hi:[0,1]
	v_pk_mul_f32 v[14:15], v[152:153], v[14:15] op_sel_hi:[0,1]
	v_pk_mul_f32 v[18:19], v[152:153], v[18:19] op_sel_hi:[0,1]
	v_mul_f32_e32 v100, v152, v3
	v_pk_fma_f32 v[10:11], v[68:69], v[178:179], v[10:11] op_sel_hi:[0,1,1]
	v_pk_fma_f32 v[14:15], v[68:69], v[74:75], v[14:15] op_sel_hi:[0,1,1]
	v_pk_fma_f32 v[18:19], v[68:69], v[90:91], v[18:19] op_sel_hi:[0,1,1]
	v_mov_b32_e32 v69, v152
	s_waitcnt lgkmcnt(1)
	v_mov_b32_e32 v24, v145
	v_mov_b32_e32 v145, v147
	s_waitcnt lgkmcnt(0)
	v_mov_b32_e32 v147, v150
	v_pk_mul_f32 v[36:37], v[50:51], v[36:37] op_sel_hi:[0,1]
	v_pk_mul_f32 v[40:41], v[50:51], v[40:41] op_sel_hi:[0,1]
	v_pk_mul_f32 v[104:105], v[162:163], v[104:105] op_sel_hi:[0,1]
	v_pk_mul_f32 v[106:107], v[166:167], v[106:107] op_sel_hi:[0,1]
	v_pk_mul_f32 v[116:117], v[162:163], v[116:117] op_sel_hi:[0,1]
	v_pk_mul_f32 v[132:133], v[162:163], v[132:133] op_sel_hi:[0,1]
	v_mul_f32_e32 v150, v156, v27
	v_pk_fma_f32 v[34:35], v[154:155], v[98:99], v[34:35] op_sel_hi:[0,1,1]
	v_pk_fma_f32 v[38:39], v[154:155], v[78:79], v[38:39] op_sel_hi:[0,1,1]
	v_pk_fma_f32 v[42:43], v[154:155], v[94:95], v[42:43] op_sel_hi:[0,1,1]
	v_mov_b32_e32 v155, v156
	s_waitcnt vmcnt(16)
; #define LAS __attribute__((address_space(3)))
; __device__ __forceinline__ unsigned cvt_pk_bf16(float lo, float hi) { unsigned r; asm("v_cvt_pk_bf16_f32 %0, %1, %2" : "=v"(r) : "v"(lo), "v"(hi)); return r; }
; template <int MODE>
; __device__ __forceinline__ void phase_prologue(const Ctx& P, LAS unsigned char* lds, int vcu, int G) {
;     ...
;         for (int d4 = 0; d4 < 64; ++d4) { const f32x4 wv = (f32x4){wo[(size_t)(4 * d4) * DM], wo[(size_t)(4 * d4 + 1) * DM], wo[(size_t)(4 * d4 + 2) * DM], wo[(size_t)(4 * d4 + 3) * DM]};
; #pragma unroll
;             for (int cc = 0; cc < 8; ++cc) { const f32x4 p4 = *(const LAS f32x4*)(pwl + cc * 256 + 4 * d4); a[cc] += (p4[0] * wv[0] + p4[1] * wv[1]) + (p4[2] * wv[2] + p4[3] * wv[3]); } }
;         u32x4 w; w.x = cvt_pk_bf16(a[0], a[1]); w.y = cvt_pk_bf16(a[2], a[3]); w.z = cvt_pk_bf16(a[4], a[5]); w.w = cvt_pk_bf16(a[6], a[7]);
;         *(u32x4*)((bf16_t*)(ws + WS_WEOUT) + (size_t)n * DM + g * 256 + c0) = w;
;         asm volatile("s_waitcnt lgkmcnt(0)" ::: "memory");
;     }
	v_pk_mul_f32 v[12:13], v[66:67], v[12:13] op_sel_hi:[0,1]
	v_pk_mul_f32 v[16:17], v[66:67], v[16:17] op_sel_hi:[0,1]
	v_pk_mul_f32 v[20:21], v[66:67], v[20:21] op_sel_hi:[0,1]
	v_pk_fma_f32 v[2:3], v[68:69], v[2:3], v[100:101] op_sel_hi:[1,1,0]
	v_mov_b32_e32 v69, v66
	v_mov_b32_e32 v129, v138
	v_mov_b32_e32 v138, v131
	v_mov_b32_e32 v131, v8
	v_mov_b32_e32 v8, v23
	v_mov_b32_e32 v23, v25
	v_pk_mul_f32 v[118:119], v[166:167], v[118:119] op_sel_hi:[0,1]
	v_pk_mul_f32 v[46:47], v[168:169], v[46:47] op_sel_hi:[0,1]
	v_pk_mul_f32 v[48:49], v[174:175], v[48:49] op_sel_hi:[0,1]
	v_pk_mul_f32 v[120:121], v[168:169], v[120:121] op_sel_hi:[0,1]
	v_pk_mul_f32 v[136:137], v[168:169], v[136:137] op_sel_hi:[0,1]
	v_mul_f32_e32 v180, v50, v29
	v_mul_f32_e32 v182, v162, v31
	v_pk_fma_f32 v[36:37], v[158:159], v[76:77], v[36:37] op_sel_hi:[0,1,1]
	v_pk_fma_f32 v[40:41], v[158:159], v[92:93], v[40:41] op_sel_hi:[0,1,1]
	v_pk_fma_f32 v[76:77], v[160:161], v[102:103], v[104:105] op_sel_hi:[0,1,1]
	v_pk_fma_f32 v[78:79], v[164:165], v[80:81], v[106:107] op_sel_hi:[0,1,1]
	v_pk_fma_f32 v[80:81], v[160:161], v[82:83], v[116:117] op_sel_hi:[0,1,1]
	v_pk_fma_f32 v[92:93], v[160:161], v[110:111], v[132:133] op_sel_hi:[0,1,1]
	v_mov_b32_e32 v159, v50
	v_mov_b32_e32 v161, v162
	v_mov_b32_e32 v153, v176
	v_pk_fma_f32 v[26:27], v[154:155], v[26:27], v[150:151] op_sel_hi:[1,1,0]
	v_mov_b32_e32 v155, v50
	v_mul_f32_e32 v50, v66, v5
	v_pk_fma_f32 v[12:13], v[176:177], v[72:73], v[12:13] op_sel_hi:[0,1,1]
	v_pk_fma_f32 v[16:17], v[176:177], v[88:89], v[16:17] op_sel_hi:[0,1,1]
	v_pk_fma_f32 v[20:21], v[176:177], v[96:97], v[20:21] op_sel_hi:[0,1,1]
	v_mov_b32_e32 v177, v66
	v_pk_mul_f32 v[6:7], v[68:69], v[6:7]
	v_pk_mul_f32 v[134:135], v[166:167], v[134:135] op_sel_hi:[0,1]
	v_mov_b32_e32 v157, v158
	v_mul_f32_e32 v186, v168, v141
	v_pk_fma_f32 v[82:83], v[164:165], v[108:109], v[118:119] op_sel_hi:[0,1,1]
	v_pk_fma_f32 v[46:47], v[170:171], v[126:127], v[46:47] op_sel_hi:[0,1,1]
	v_pk_fma_f32 v[48:49], v[172:173], v[84:85], v[48:49] op_sel_hi:[0,1,1]
	v_pk_fma_f32 v[84:85], v[170:171], v[86:87], v[120:121] op_sel_hi:[0,1,1]
	v_pk_fma_f32 v[98:99], v[170:171], v[114:115], v[136:137] op_sel_hi:[0,1,1]
	v_mov_b32_e32 v171, v168
	v_pk_fma_f32 v[30:31], v[160:161], v[30:31], v[182:183] op_sel_hi:[1,1,0]
	v_mov_b32_e32 v161, v166
	v_pk_mul_f32 v[22:23], v[154:155], v[22:23]
	v_pk_fma_f32 v[4:5], v[176:177], v[4:5], v[50:51] op_sel_hi:[1,1,0]
	v_pk_fma_f32 v[6:7], v[152:153], v[130:131], v[6:7]
	v_mov_b32_e32 v25, v146
	v_mov_b32_e32 v146, v149
	v_mov_b32_e32 v149, v151
	v_pk_mul_f32 v[122:123], v[174:175], v[122:123] op_sel_hi:[0,1]
	v_pk_mul_f32 v[138:139], v[174:175], v[138:139] op_sel_hi:[0,1]
	v_mul_f32_e32 v184, v166, v33
	v_mov_b32_e32 v163, v164
	v_pk_fma_f32 v[94:95], v[164:165], v[124:125], v[134:135] op_sel_hi:[0,1,1]
	v_mov_b32_e32 v165, v166
	v_pk_add_f32 v[34:35], v[34:35], v[36:37]
	v_pk_add_f32 v[36:37], v[38:39], v[40:41]
	v_pk_add_f32 v[38:39], v[42:43], v[44:45]
	v_pk_fma_f32 v[28:29], v[158:159], v[28:29], v[180:181] op_sel_hi:[1,1,0]
	v_pk_add_f32 v[40:41], v[76:77], v[78:79]
	v_pk_add_f32 v[42:43], v[80:81], v[82:83]
	v_pk_fma_f32 v[76:77], v[170:171], v[140:141], v[186:187] op_sel_hi:[1,1,0]
	v_mov_b32_e32 v171, v174
	v_pk_mul_f32 v[80:81], v[160:161], v[144:145]
	v_pk_fma_f32 v[8:9], v[156:157], v[8:9], v[22:23]
	v_mov_b32_e32 v3, v6
	v_mov_b32_e32 v5, v7
	v_mul_f32_e32 v188, v174, v143
	v_mov_b32_e32 v169, v172
	v_pk_fma_f32 v[86:87], v[172:173], v[112:113], v[122:123] op_sel_hi:[0,1,1]
	v_pk_fma_f32 v[102:103], v[172:173], v[128:129], v[138:139] op_sel_hi:[0,1,1]
	v_mov_b32_e32 v173, v174
	v_pk_fma_f32 v[32:33], v[164:165], v[32:33], v[184:185] op_sel_hi:[1,1,0]
	v_pk_mul_f32 v[82:83], v[170:171], v[148:149]
	v_pk_fma_f32 v[22:23], v[162:163], v[24:25], v[80:81]
	v_pk_add_f32 v[10:11], v[10:11], v[12:13]
	v_pk_add_f32 v[12:13], v[14:15], v[16:17]
	v_pk_add_f32 v[14:15], v[18:19], v[20:21]
	v_mov_b32_e32 v27, v8
	v_mov_b32_e32 v29, v9
	v_pk_add_f32 v[2:3], v[2:3], v[4:5]
	v_pk_fma_f32 v[78:79], v[172:173], v[142:143], v[188:189] op_sel_hi:[1,1,0]
	v_pk_fma_f32 v[24:25], v[168:169], v[146:147], v[82:83]
	v_mov_b32_e32 v31, v22
	v_mov_b32_e32 v33, v23
	v_pk_add_f32 v[8:9], v[60:61], v[10:11]
	v_pk_add_f32 v[10:11], v[64:65], v[12:13]
	v_pk_add_f32 v[12:13], v[62:63], v[14:15]
	v_pk_add_f32 v[6:7], v[26:27], v[28:29]
	v_pk_add_f32 v[2:3], v[56:57], v[2:3]
	v_pk_add_f32 v[44:45], v[92:93], v[94:95]
	v_mov_b32_e32 v77, v24
	v_mov_b32_e32 v79, v25
	v_pk_add_f32 v[14:15], v[30:31], v[32:33]
	v_pk_add_f32 v[4:5], v[8:9], v[34:35]
	v_pk_add_f32 v[8:9], v[10:11], v[36:37]
	v_pk_add_f32 v[10:11], v[12:13], v[38:39]
	v_pk_add_f32 v[2:3], v[2:3], v[6:7]
	s_add_i32 s4, s4, 64
	v_pk_add_f32 v[46:47], v[46:47], v[48:49]
	v_pk_add_f32 v[48:49], v[84:85], v[86:87]
	v_pk_add_f32 v[74:75], v[98:99], v[102:103]
	v_pk_add_f32 v[16:17], v[76:77], v[78:79]
	v_pk_add_f32 v[4:5], v[4:5], v[40:41]
	v_pk_add_f32 v[8:9], v[8:9], v[42:43]
	v_pk_add_f32 v[10:11], v[10:11], v[44:45]
	v_pk_add_f32 v[2:3], v[2:3], v[14:15]
	s_cmp_eq_u32 s14, 0x200000
	v_pk_add_f32 v[60:61], v[4:5], v[46:47]
	v_pk_add_f32 v[64:65], v[8:9], v[48:49]
	v_pk_add_f32 v[62:63], v[10:11], v[74:75]
	v_pk_add_f32 v[56:57], v[2:3], v[16:17]
	s_cbranch_scc0 .LBB0_294
	s_lshl_b32 s2, s9, 6
	s_and_b32 s2, s2, 0x7c0
	v_or_b32_e32 v6, s2, v1
	v_lshlrev_b32_e32 v50, 12, v6
	v_lshl_add_u64 v[6:7], s[6:7], 0, v[50:51]
	s_lshl_b32 s4, s40, 1
	v_lshl_add_u64 v[6:7], v[6:7], 0, s[4:5]
	v_lshl_add_u64 v[6:7], s[12:13], 1, v[6:7]
	v_cvt_pk_bf16_f32 v2, v60, v61
	v_cvt_pk_bf16_f32 v3, v64, v65
	v_cvt_pk_bf16_f32 v4, v62, v63
	v_cvt_pk_bf16_f32 v5, v56, v57
	global_store_dwordx4 v[6:7], v[2:5], off
	s_waitcnt lgkmcnt(0)
	s_add_i32 s9, s9, s16
	s_add_i32 s18, s18, s19
	s_add_i32 s20, s20, s21
	s_cmpk_gt_i32 s9, 0xfff
	s_cbranch_scc0 .LBB0_293
